# Also defers 1024 layer-0 MoE up-projection weight tiles from the prologue to the workgroups idle during top-k L0 (second small conversion queue, drained before the MoE GEMM)
# baseline (speedup 1.0000x reference)
; #define LAS __attribute__((address_space(3)))
; __device__ __forceinline__ void phase_prologue(const Args& a, LAS unsigned char* lds) {
;     ...
;     unsigned* cq_head = (unsigned*)(a.ws + WS_CTL) + 8192 + 768;
;     volatile LAS int* qs = (volatile LAS int*)(lds + 128 * 129 * 4);
;     int pend = 0, it = 0;
;     if (tid == 0) { qs[0] = (int)xb_add(cq_head, 1u); pend = (int)xb_add(cq_head, 1u); }
;     __syncthreads();
;     for (int u = qs[0]; u < CTOT; u = qs[it & 1]) {
;         int r = u; const float* src; int ldn, nvalid, NT, mode = 0; bf16_t* dst;
;         if (r < CJ0) { src = a.in[I_EVIN]; ldn = 6144; nvalid = 6144; NT = 48; dst = (bf16_t*)(a.ws + WS_WIN0); }
;         else if ((r -= CJ0) < CJ1) { src = a.in[I_EVOUT]; ldn = 2048; nvalid = 2048; NT = 16; dst = (bf16_t*)(a.ws + WS_WOUT0); }
;         else if ((r -= CJ1) < CJ2) { src = a.in[I_ODIN]; ldn = 6176; nvalid = 6176; NT = 50; dst = (bf16_t*)(a.ws + WS_WIN1); }
;         else if ((r -= CJ2) < CJ3) { src = a.in[I_ODOUT]; ldn = 2048; nvalid = 2048; NT = 16; dst = (bf16_t*)(a.ws + WS_WOUT1); }
;         else { r -= CJ3; const int which = r / CJM; r -= which * CJM; const int mtx = r >> 8; r &= 255; ldn = 2048; nvalid = 2048; NT = 16;
;             if (which == 0) { src = a.in[I_WGATE] + (size_t)mtx * 2048 * 2048; dst = (bf16_t*)(a.ws + WS_WGU) + (size_t)mtx * 4096 * 2048; mode = 1; }
;             else if (which == 1) { src = a.in[I_WUP] + (size_t)mtx * 2048 * 2048; dst = (bf16_t*)(a.ws + WS_WGU) + (size_t)mtx * 4096 * 2048; mode = 2; }
;             else { src = a.in[I_WDOWN] + (size_t)mtx * 2048 * 2048; dst = (bf16_t*)(a.ws + WS_WDN) + (size_t)mtx * 2048 * 2048; } }
;         const int kt = r / NT, ntl = r % NT, k0 = kt * 128, n0 = ntl * 128;
;         const int drow0 = mode == 0 ? n0 : (ntl * 256 + (mode == 2 ? 128 : 0));
;         f32x4 v[8];
; #pragma unroll
;         for (int i = 0; i < 8; ++i) { const int id = tid + 512 * i, row = id >> 5, c4 = id & 31, n = n0 + c4 * 4;
;             v[i] = (f32x4){0.f, 0.f, 0.f, 0.f};
;             if (n < nvalid) v[i] = *(const f32x4*)(src + (size_t)(k0 + row) * ldn + n); }
; #pragma unroll
;         for (int i = 0; i < 8; ++i) { const int id = tid + 512 * i, row = id >> 5, c4 = id & 31;
;             LAS float* tp = tile + row * 129 + c4 * 4; tp[0] = v[i][0]; tp[1] = v[i][1]; tp[2] = v[i][2]; tp[3] = v[i][3]; }
;         lds_barrier();
; #pragma unroll
.LBB0_37:
	s_or_b64 exec, exec, s[6:7]
	s_add_i32 s6, 0, 0x10200
	v_mov_b32_e32 v2, s6
	s_waitcnt lgkmcnt(0)
	s_barrier
	ds_read_b32 v2, v2
	s_movk_i32 s6, 0x241f
	s_waitcnt lgkmcnt(0)
	v_cmp_lt_i32_e32 vcc, s6, v2
	v_readfirstlane_b32 s20, v2
	s_cbranch_vccnz .LBB0_79
	v_lshlrev_b32_e32 v2, 3, v0
	v_or_b32_e32 v6, 0xa00, v0
	v_and_b32_e32 v2, 0x78, v2
	s_movk_i32 s6, 0x204
	v_or_b32_e32 v4, 0x200, v0
	v_or_b32_e32 v5, 0x600, v0
	v_lshrrev_b32_e32 v40, 5, v6
	v_or_b32_e32 v6, 0xe00, v0
	v_or_b32_e32 v8, 0x400, v0
	v_mad_u32_u24 v3, v2, s6, 0
	v_lshrrev_b32_e32 v38, 5, v4
	v_lshrrev_b32_e32 v39, 5, v5
	v_lshrrev_b32_e32 v41, 5, v6
	v_lshrrev_b32_e32 v9, 5, v8
	v_lshrrev_b32_e32 v42, 4, v0
	v_lshrrev_b32_e32 v44, 4, v4
	v_lshrrev_b32_e32 v46, 4, v8
	v_lshrrev_b32_e32 v48, 4, v5
	v_mul_u32_u24_e32 v6, 0x204, v104
	v_mul_u32_u24_e32 v7, 0x204, v38
	v_mul_u32_u24_e32 v9, 0x204, v9
	v_mul_u32_u24_e32 v10, 0x204, v39
	v_mul_u32_u24_e32 v11, 0x204, v40
	v_lshl_add_u32 v43, v42, 2, v3
	v_lshl_add_u32 v45, v44, 2, v3
	v_lshl_add_u32 v47, v46, 2, v3
	v_lshl_add_u32 v49, v48, 2, v3
	v_mul_u32_u24_e32 v3, 0x204, v41
	v_mov_b32_e32 v35, 0
	v_or_b32_e32 v50, 32, v104
	v_or_b32_e32 v51, 64, v104
	v_or_b32_e32 v52, 0x60, v104
	s_mov_b32 s16, 1
	v_add_u32_e32 v53, v106, v6
	v_add_u32_e32 v54, v106, v7
	v_add_u32_e32 v55, v106, v9
	v_add_u32_e32 v56, v106, v10
	v_add_u32_e32 v57, v106, v11
	v_add_u32_e32 v58, v106, v3
	v_lshlrev_b32_e32 v34, 1, v2
	s_movk_i32 s17, 0x2420
	s_branch .LBB0_41

; #define LAS __attribute__((address_space(3)))
; __device__ __forceinline__ void phase_prologue(const Args& a, LAS unsigned char* lds) {
;     ...
;     unsigned* cq_head = (unsigned*)(a.ws + WS_CTL) + 8192 + 768;
;     volatile LAS int* qs = (volatile LAS int*)(lds + 128 * 129 * 4);
;     int pend = 0, it = 0;
;     if (tid == 0) { qs[0] = (int)xb_add(cq_head, 1u); pend = (int)xb_add(cq_head, 1u); }
;     __syncthreads();
;     for (int u = qs[0]; u < CTOT; u = qs[it & 1]) {
;         int r = u; const float* src; int ldn, nvalid, NT, mode = 0; bf16_t* dst;
;         if (r < CJ0) { src = a.in[I_EVIN]; ldn = 6144; nvalid = 6144; NT = 48; dst = (bf16_t*)(a.ws + WS_WIN0); }
;         else if ((r -= CJ0) < CJ1) { src = a.in[I_EVOUT]; ldn = 2048; nvalid = 2048; NT = 16; dst = (bf16_t*)(a.ws + WS_WOUT0); }
;         else if ((r -= CJ1) < CJ2) { src = a.in[I_ODIN]; ldn = 6176; nvalid = 6176; NT = 50; dst = (bf16_t*)(a.ws + WS_WIN1); }
;         else if ((r -= CJ2) < CJ3) { src = a.in[I_ODOUT]; ldn = 2048; nvalid = 2048; NT = 16; dst = (bf16_t*)(a.ws + WS_WOUT1); }
;         else { r -= CJ3; const int which = r / CJM; r -= which * CJM; const int mtx = r >> 8; r &= 255; ldn = 2048; nvalid = 2048; NT = 16;
;             if (which == 0) { src = a.in[I_WGATE] + (size_t)mtx * 2048 * 2048; dst = (bf16_t*)(a.ws + WS_WGU) + (size_t)mtx * 4096 * 2048; mode = 1; }
;             else if (which == 1) { src = a.in[I_WUP] + (size_t)mtx * 2048 * 2048; dst = (bf16_t*)(a.ws + WS_WGU) + (size_t)mtx * 4096 * 2048; mode = 2; }
;             else { src = a.in[I_WDOWN] + (size_t)mtx * 2048 * 2048; dst = (bf16_t*)(a.ws + WS_WDN) + (size_t)mtx * 2048 * 2048; } }
;         const int kt = r / NT, ntl = r % NT, k0 = kt * 128, n0 = ntl * 128;
;         const int drow0 = mode == 0 ? n0 : (ntl * 256 + (mode == 2 ? 128 : 0));
;         f32x4 v[8];
; #pragma unroll
;         for (int i = 0; i < 8; ++i) { const int id = tid + 512 * i, row = id >> 5, c4 = id & 31, n = n0 + c4 * 4;
;             v[i] = (f32x4){0.f, 0.f, 0.f, 0.f};
;             if (n < nvalid) v[i] = *(const f32x4*)(src + (size_t)(k0 + row) * ldn + n); }
; #pragma unroll
;         for (int i = 0; i < 8; ++i) { const int id = tid + 512 * i, row = id >> 5, c4 = id & 31;
;             LAS float* tp = tile + row * 129 + c4 * 4; tp[0] = v[i][0]; tp[1] = v[i][1]; tp[2] = v[i][2]; tp[3] = v[i][3]; }
;         lds_barrier();
; #pragma unroll
.LBB0_768:
.Lcvq0_entry:
	s_waitcnt vmcnt(0) lgkmcnt(0)
	s_barrier
	v_mov_b32_e32 v119, 1
	v_mov_b32_e32 v120, 0x9080
	v_mov_b32_e32 v122, 0
	v_mov_b32_e32 v125, 0x10200
	s_mov_b32 s67, 0
	v_lshrrev_b32_e32 v104, 5, v0
	v_and_b32_e32 v126, 31, v0
	v_lshlrev_b32_e32 v105, 13, v104
	v_lshl_add_u32 v105, v126, 4, v105
	v_add_u32_e32 v106, 0x20000, v105
	v_add_u32_e32 v107, 0x40000, v105
	v_add_u32_e32 v108, 0x60000, v105
	v_add_u32_e32 v109, 0x80000, v105
	v_add_u32_e32 v110, 0xa0000, v105
	v_add_u32_e32 v111, 0xc0000, v105
	v_add_u32_e32 v112, 0xe0000, v105
	v_mul_u32_u24_e32 v113, 0x204, v104
	v_lshl_add_u32 v113, v126, 4, v113
	v_lshrrev_b32_e32 v127, 4, v0
	v_and_b32_e32 v126, 15, v0
	v_mul_u32_u24_e32 v114, 0x1020, v126
	v_lshl_add_u32 v114, v127, 2, v114
	v_lshlrev_b32_e32 v115, 12, v127
	v_lshl_add_u32 v115, v126, 4, v115
	v_add_u32_e32 v116, 0x20000, v115
	v_add_u32_e32 v117, 0x40000, v115
	v_add_u32_e32 v118, 0x60000, v115
	v_readlane_b32 s82, v254, 27
	v_readlane_b32 s83, v254, 28
	s_sub_u32 s82, s82, 0x28
	s_subb_u32 s83, s83, 0
	s_load_dwordx2 s[80:81], s[82:83], 0x0
	s_waitcnt lgkmcnt(0)
	v_cmp_eq_u32_e32 vcc, 0, v0
	s_and_saveexec_b64 s[76:77], vcc
	s_cbranch_execz .Lcvq0_t0a
	global_atomic_add v123, v120, v119, s[94:95] sc0
	s_waitcnt vmcnt(0)
	ds_write_b32 v125, v123

; __device__ __forceinline__ void phase_prologue(const Args& a, LAS unsigned char* lds) {
;     ...
;         int r = u; const float* src; int ldn, nvalid, NT, mode = 0; bf16_t* dst;
;         if (r < CJ0) { src = a.in[I_EVIN]; ldn = 6144; nvalid = 6144; NT = 48; dst = (bf16_t*)(a.ws + WS_WIN0); }
;         else if ((r -= CJ0) < CJ1) { src = a.in[I_EVOUT]; ldn = 2048; nvalid = 2048; NT = 16; dst = (bf16_t*)(a.ws + WS_WOUT0); }
;         else if ((r -= CJ1) < CJ2) { src = a.in[I_ODIN]; ldn = 6176; nvalid = 6176; NT = 50; dst = (bf16_t*)(a.ws + WS_WIN1); }
;         else if ((r -= CJ2) < CJ3) { src = a.in[I_ODOUT]; ldn = 2048; nvalid = 2048; NT = 16; dst = (bf16_t*)(a.ws + WS_WOUT1); }
;         else { r -= CJ3; const int which = r / CJM; r -= which * CJM; const int mtx = r >> 8; r &= 255; ldn = 2048; nvalid = 2048; NT = 16;
;             if (which == 0) { src = a.in[I_WGATE] + (size_t)mtx * 2048 * 2048; dst = (bf16_t*)(a.ws + WS_WGU) + (size_t)mtx * 4096 * 2048; mode = 1; }
;             else if (which == 1) { src = a.in[I_WUP] + (size_t)mtx * 2048 * 2048; dst = (bf16_t*)(a.ws + WS_WGU) + (size_t)mtx * 4096 * 2048; mode = 2; }
;             else { src = a.in[I_WDOWN] + (size_t)mtx * 2048 * 2048; dst = (bf16_t*)(a.ws + WS_WDN) + (size_t)mtx * 2048 * 2048; } }
;         const int kt = r / NT, ntl = r % NT, k0 = kt * 128, n0 = ntl * 128;
;         const int drow0 = mode == 0 ? n0 : (ntl * 256 + (mode == 2 ? 128 : 0));
;         f32x4 v[8];
; #pragma unroll
;         for (int i = 0; i < 8; ++i) { const int id = tid + 512 * i, row = id >> 5, c4 = id & 31, n = n0 + c4 * 4;
;             v[i] = (f32x4){0.f, 0.f, 0.f, 0.f};
;             if (n < nvalid) v[i] = *(const f32x4*)(src + (size_t)(k0 + row) * ldn + n); }
; #pragma unroll
;         for (int i = 0; i < 8; ++i) { const int id = tid + 512 * i, row = id >> 5, c4 = id & 31;
;             LAS float* tp = tile + row * 129 + c4 * 4; tp[0] = v[i][0]; tp[1] = v[i][1]; tp[2] = v[i][2]; tp[3] = v[i][3]; }
;         lds_barrier();
; #pragma unroll
;         for (int i = 0; i < 4; ++i) { const int piece = tid + 512 * i, nl = piece >> 4, kg = piece & 15; const LAS float* s = tile + (kg * 8) * 129 + nl;
;             u32x4 o; o.x = pk2(s[0], s[129]); o.y = pk2(s[258], s[387]); o.z = pk2(s[516], s[645]); o.w = pk2(s[774], s[903]);
;             *(u32x4*)(dst + (size_t)(drow0 + nl) * 2048 + k0 + kg * 8) = o; }
;         ++it;
.Lcvq0_loop:
	ds_read_b32 v126, v125
	s_waitcnt lgkmcnt(0)
	v_readfirstlane_b32 s66, v126
	s_cmpk_gt_u32 s66, 0x3ff
	s_cbranch_scc1 .Lcvq0_done
	v_cmp_eq_u32_e32 vcc, 0, v0
	s_and_saveexec_b64 s[76:77], vcc
	s_cbranch_execz .Lcvq0_t0b
	global_atomic_add v123, v120, v119, s[94:95] sc0
.Lcvq0_t0b:
	s_mov_b64 exec, s[76:77]
	s_mov_b32 s78, 1
	s_bfe_u32 s72, s66, 0x20008
	s_add_i32 s72, s72, 12
	s_lshl_b32 s72, s72, 24
	s_bfe_u32 s73, s66, 0x40004
	s_and_b32 s74, s66, 15
	v_readlane_b32 s68, v254, 43
	v_readlane_b32 s69, v254, 44
	s_cmp_lg_u32 s78, 0
	s_cselect_b32 s68, s80, s68
	s_cselect_b32 s69, s81, s69
	s_lshl_b32 s75, s73, 20
	s_add_i32 s75, s75, s72
	s_lshl_b32 s79, s74, 9
	s_add_i32 s75, s75, s79
	s_add_u32 s68, s68, s75
	s_addc_u32 s69, s69, 0
	v_readlane_b32 s70, v254, 25
	v_readlane_b32 s71, v254, 26
	s_lshl_b32 s75, s74, 20
	s_add_i32 s75, s75, s72
	s_lshl_b32 s79, s78, 19
	s_add_i32 s75, s75, s79
	s_lshl_b32 s79, s73, 8
	s_add_i32 s75, s75, s79
	s_add_u32 s70, s70, s75
	s_addc_u32 s71, s71, 0
	global_load_dwordx4 v[128:131], v105, s[68:69]
	global_load_dwordx4 v[132:135], v106, s[68:69]
	global_load_dwordx4 v[136:139], v107, s[68:69]
	global_load_dwordx4 v[140:143], v108, s[68:69]
	global_load_dwordx4 v[144:147], v109, s[68:69]
	global_load_dwordx4 v[148:151], v110, s[68:69]
	global_load_dwordx4 v[152:155], v111, s[68:69]
	global_load_dwordx4 v[156:159], v112, s[68:69]
	s_waitcnt vmcnt(7)
	ds_write_b32 v113, v128
	ds_write_b32 v113, v129 offset:4
	ds_write_b32 v113, v130 offset:8
	ds_write_b32 v113, v131 offset:12
	s_waitcnt vmcnt(6)
	ds_write_b32 v113, v132 offset:8256
	ds_write_b32 v113, v133 offset:8260
	ds_write_b32 v113, v134 offset:8264
	ds_write_b32 v113, v135 offset:8268
	s_waitcnt vmcnt(5)
	ds_write_b32 v113, v136 offset:16512
	ds_write_b32 v113, v137 offset:16516
	ds_write_b32 v113, v138 offset:16520
	ds_write_b32 v113, v139 offset:16524
	s_waitcnt vmcnt(4)
	ds_write_b32 v113, v140 offset:24768
	ds_write_b32 v113, v141 offset:24772
	ds_write_b32 v113, v142 offset:24776
	ds_write_b32 v113, v143 offset:24780
	s_waitcnt vmcnt(3)
	ds_write_b32 v113, v144 offset:33024
	ds_write_b32 v113, v145 offset:33028
	ds_write_b32 v113, v146 offset:33032
	ds_write_b32 v113, v147 offset:33036
	s_waitcnt vmcnt(2)
	ds_write_b32 v113, v148 offset:41280
	ds_write_b32 v113, v149 offset:41284
	ds_write_b32 v113, v150 offset:41288
	ds_write_b32 v113, v151 offset:41292
	s_waitcnt vmcnt(1)
	ds_write_b32 v113, v152 offset:49536
	ds_write_b32 v113, v153 offset:49540
	ds_write_b32 v113, v154 offset:49544
	ds_write_b32 v113, v155 offset:49548
	s_waitcnt vmcnt(0)
	ds_write_b32 v113, v156 offset:57792
	ds_write_b32 v113, v157 offset:57796
	ds_write_b32 v113, v158 offset:57800
	ds_write_b32 v113, v159 offset:57804
	s_waitcnt lgkmcnt(0)
	s_barrier
	ds_read_b32 v160, v114
	ds_read_b32 v161, v114 offset:516
	ds_read_b32 v162, v114 offset:1032
	ds_read_b32 v163, v114 offset:1548
	ds_read_b32 v164, v114 offset:2064
	ds_read_b32 v165, v114 offset:2580
	ds_read_b32 v166, v114 offset:3096
	ds_read_b32 v167, v114 offset:3612
	s_waitcnt lgkmcnt(0)
	v_cvt_pk_bf16_f32 v168, v160, v161
	v_cvt_pk_bf16_f32 v169, v162, v163
	v_cvt_pk_bf16_f32 v170, v164, v165
	v_cvt_pk_bf16_f32 v171, v166, v167
	global_store_dwordx4 v115, v[168:171], s[70:71]
	ds_read_b32 v160, v114 offset:128
	ds_read_b32 v161, v114 offset:644
	ds_read_b32 v162, v114 offset:1160
	ds_read_b32 v163, v114 offset:1676
	ds_read_b32 v164, v114 offset:2192
	ds_read_b32 v165, v114 offset:2708
	ds_read_b32 v166, v114 offset:3224
	ds_read_b32 v167, v114 offset:3740
	s_waitcnt lgkmcnt(0)
	v_cvt_pk_bf16_f32 v172, v160, v161
	v_cvt_pk_bf16_f32 v173, v162, v163
	v_cvt_pk_bf16_f32 v174, v164, v165
	v_cvt_pk_bf16_f32 v175, v166, v167
	global_store_dwordx4 v116, v[172:175], s[70:71]
	ds_read_b32 v160, v114 offset:256
	ds_read_b32 v161, v114 offset:772
	ds_read_b32 v162, v114 offset:1288
	ds_read_b32 v163, v114 offset:1804
	ds_read_b32 v164, v114 offset:2320
	ds_read_b32 v165, v114 offset:2836
	ds_read_b32 v166, v114 offset:3352
	ds_read_b32 v167, v114 offset:3868
	s_waitcnt lgkmcnt(0)
	v_cvt_pk_bf16_f32 v168, v160, v161
	v_cvt_pk_bf16_f32 v169, v162, v163
	v_cvt_pk_bf16_f32 v170, v164, v165
	v_cvt_pk_bf16_f32 v171, v166, v167
	global_store_dwordx4 v117, v[168:171], s[70:71]
	ds_read_b32 v160, v114 offset:384
	ds_read_b32 v161, v114 offset:900
	ds_read_b32 v162, v114 offset:1416
	ds_read_b32 v163, v114 offset:1932
	ds_read_b32 v164, v114 offset:2448
	ds_read_b32 v165, v114 offset:2964
	ds_read_b32 v166, v114 offset:3480
	ds_read_b32 v167, v114 offset:3996
	s_waitcnt lgkmcnt(0)
	v_cvt_pk_bf16_f32 v172, v160, v161
	v_cvt_pk_bf16_f32 v173, v162, v163
	v_cvt_pk_bf16_f32 v174, v164, v165
	v_cvt_pk_bf16_f32 v175, v166, v167
	global_store_dwordx4 v118, v[172:175], s[70:71]
	v_cmp_eq_u32_e32 vcc, 0, v0
	s_and_saveexec_b64 s[76:77], vcc
	s_cbranch_execz .Lcvq0_t0c
	s_waitcnt vmcnt(0)
	ds_write_b32 v125, v123
.Lcvq0_t0c:
	s_mov_b64 exec, s[76:77]
	s_waitcnt lgkmcnt(0)
	s_barrier
	s_branch .Lcvq0_loop
.Lcvq0_done:
.Lcvd_entry:
	s_waitcnt vmcnt(0) lgkmcnt(0)
	s_barrier
	v_mov_b32_e32 v119, 1
	v_mov_b32_e32 v120, 0x9000
	v_mov_b32_e32 v121, 0x9200
	v_mov_b32_e32 v122, 0
	v_mov_b32_e32 v125, 0x10200
	s_mov_b32 s67, 0
	v_cmp_eq_u32_e32 vcc, 0, v0
	s_and_saveexec_b64 s[76:77], vcc
	s_cbranch_execz .Lcvd_f0
	global_atomic_add v124, v121, v119, s[94:95] sc0
	s_waitcnt vmcnt(0)
	v_add_u32_e32 v124, 1, v124
	ds_write_b32 v125, v124 offset:4
